# fin phase: the 7 per-token global loads (chain output fwd/bwd, gate, bonus scalar, token-shift rows) issued together into separate registers instead of 4 serialized round trips
# speedup vs baseline: 1.0051x; 1.0034x over previous
; DI void unpack8(const u32x4 w, float (&o)[8]) { o[0] = bf2f(w.x & 0xffffu); o[1] = bf2f(w.x >> 16); o[2] = bf2f(w.y & 0xffffu); o[3] = bf2f(w.y >> 16); o[4] = bf2f(w.z & 0xffffu); o[5] = bf2f(w.z >> 16); o[6] = bf2f(w.w & 0xffffu); o[7] = bf2f(w.w >> 16); }
; DI void phase_fin(const Frame& F, int j) {
;     ...
;     for (int t = F.gw; t < T; t += F.NGW) {
;         float yf[8], yb[8], bo[8], ga[8]; unpack8(*(const u32x4*)(YD + (size_t)t * 512 + ch0), yf); unpack8(*(const u32x4*)(YD + ((size_t)T + t) * 512 + ch0), yb); unpack8(*(const u32x4*)(LO + (size_t)t * LORA_N + 2048 + ch0), ga);
;         {
;             const int tt = t & (SEQ - 1); const bf16_t* pr = P + (size_t)t * AB_PROJ + 1024 + ch0; const float bs = BS[(size_t)t * 8 + (F.lane >> 3)];
;             float c[8], pv[8], nv[8]; unpack8(*(const u32x4*)pr, c); unpack8(*(const u32x4*)(pr - (tt > 0 ? AB_PROJ : 0)), pv); unpack8(*(const u32x4*)(pr + (tt < SEQ - 1 ? AB_PROJ : 0)), nv);
; #pragma unroll
;             for (int i = 0; i < 8; ++i) { const float p0 = tt > 0 ? pv[i] : 0.f, n0 = tt < SEQ - 1 ? nv[i] : 0.f; bo[i] = bs * (c[i] + mp[i] * (p0 - c[i]) + mn[i] * (n0 - c[i])); } }
;         float s = 0.f;
; #pragma unroll
;         for (int i = 0; i < 8; ++i) { yf[i] += yb[i]; s += yf[i]; }
.LBB0_823:
	v_lshl_add_u64 v[60:61], s[44:45], 0, v[44:45]
	global_load_dwordx4 v[60:63], v[60:61], off
	v_lshl_add_u64 v[56:57], s[44:45], 0, v[46:47]
	v_add_co_u32_e32 v52, vcc, 0xd7000000, v56
	s_and_b32 s2, s40, 0xfff
	s_nop 0
	v_addc_co_u32_e32 v53, vcc, 0, v57, vcc
	v_add_co_u32_e32 v56, vcc, 0xd9000000, v56
	global_load_dwordx4 v[52:55], v[52:53], off
	s_nop 0
	v_addc_co_u32_e32 v57, vcc, 0, v57, vcc
	global_load_dwordx4 v[56:59], v[56:57], off
	s_cmp_eq_u32 s2, 0
	s_cselect_b64 s[4:5], -1, 0
	s_and_b64 s[6:7], s[4:5], exec
	s_cselect_b32 s12, 0, 0xffffea00
	s_cselect_b32 s13, 0, -1
	s_add_u32 s12, s44, s12
	s_addc_u32 s13, s45, s13
	s_cmpk_eq_i32 s2, 0xfff
	s_cselect_b64 s[6:7], -1, 0
	s_and_b64 s[8:9], s[6:7], exec
	s_cselect_b32 s2, 0, 0x1600
	s_add_u32 s8, s44, s2
	s_addc_u32 s9, s45, 0
	s_add_i32 s40, s40, s42
	s_cmp_lt_i32 s40, 0x8000
	v_lshl_add_u64 v[226:227], s[44:45], 0, v[40:41]
	v_lshl_add_u64 v[228:229], s[44:45], 0, v[42:43]
	global_load_dword v32, v[228:229], off
	global_load_dwordx4 v[194:197], v[226:227], off
	v_lshl_add_u64 v[230:231], s[12:13], 0, v[40:41]
	global_load_dwordx4 v[198:201], v[230:231], off
	v_lshl_add_u64 v[232:233], s[8:9], 0, v[40:41]
	global_load_dwordx4 v[202:205], v[232:233], off
	v_lshl_add_u64 v[44:45], v[44:45], 0, s[46:47]
	v_lshl_add_u64 v[46:47], v[46:47], 0, s[48:49]
	v_lshl_add_u64 v[42:43], v[42:43], 0, s[38:39]
	v_lshl_add_u64 v[40:41], v[40:41], 0, s[36:37]
	s_waitcnt vmcnt(6)
	v_lshlrev_b32_e32 v24, 16, v60
	v_and_b32_e32 v26, 0xffff0000, v60
	v_lshlrev_b32_e32 v28, 16, v61
	v_and_b32_e32 v30, 0xffff0000, v61
	v_lshlrev_b32_e32 v95, 16, v62
	v_and_b32_e32 v104, 0xffff0000, v62
	v_lshlrev_b32_e32 v105, 16, v63
	v_and_b32_e32 v106, 0xffff0000, v63
	s_waitcnt vmcnt(5)
	v_lshlrev_b32_e32 v101, 16, v52
	s_waitcnt vmcnt(4)
	v_lshlrev_b32_e32 v99, 16, v56
	v_and_b32_e32 v98, 0xffff0000, v56
	v_and_b32_e32 v100, 0xffff0000, v52
	v_pk_add_f32 v[98:99], v[100:101], v[98:99]
	v_lshlrev_b32_e32 v101, 16, v57
	v_lshlrev_b32_e32 v103, 16, v53
	v_and_b32_e32 v100, 0xffff0000, v57
	v_and_b32_e32 v102, 0xffff0000, v53
	v_pk_add_f32 v[52:53], v[102:103], v[100:101]
	v_lshlrev_b32_e32 v57, 16, v58
	v_lshlrev_b32_e32 v101, 16, v54
	v_and_b32_e32 v56, 0xffff0000, v58
	v_and_b32_e32 v100, 0xffff0000, v54
	v_pk_add_f32 v[56:57], v[100:101], v[56:57]
	v_lshlrev_b32_e32 v101, 16, v59
	v_lshlrev_b32_e32 v103, 16, v55
	v_and_b32_e32 v100, 0xffff0000, v59
	v_and_b32_e32 v102, 0xffff0000, v55
	v_pk_add_f32 v[54:55], v[102:103], v[100:101]
	v_mov_b32_e32 v87, v57
	v_mov_b32_e32 v93, v55
	v_mov_b32_e32 v97, v54
	v_mov_b32_e32 v85, v52
	v_mov_b32_e32 v91, v56
	s_waitcnt vmcnt(2)
	v_lshlrev_b32_e32 v66, 16, v194
	v_and_b32_e32 v68, 0xffff0000, v194
	v_lshlrev_b32_e32 v70, 16, v195
	v_and_b32_e32 v72, 0xffff0000, v195
	v_lshlrev_b32_e32 v74, 16, v196
	v_and_b32_e32 v76, 0xffff0000, v196
	v_lshlrev_b32_e32 v78, 16, v197
	v_and_b32_e32 v80, 0xffff0000, v197
	s_waitcnt vmcnt(1)
	v_lshlrev_b32_e32 v36, 16, v199
	v_and_b32_e32 v38, 0xffff0000, v199
	v_lshlrev_b32_e32 v51, 16, v200
	v_and_b32_e32 v61, 0xffff0000, v200
	v_lshlrev_b32_e32 v67, 16, v201
	v_and_b32_e32 v69, 0xffff0000, v201
	v_and_b32_e32 v34, 0xffff0000, v198
	v_cndmask_b32_e64 v34, v34, 0, s[4:5]
	v_sub_f32_e32 v34, v34, v68
	v_mul_f32_e32 v83, v9, v34
	v_lshlrev_b32_e32 v60, 16, v198
	v_cndmask_b32_e64 v60, v60, 0, s[4:5]
	v_sub_f32_e32 v60, v60, v66
	v_mul_f32_e32 v60, v8, v60
	s_waitcnt vmcnt(0)
; DI unsigned pk_fp8x4(float a, float b, float c, float d) { int p = 0; p = __builtin_amdgcn_cvt_pk_fp8_f32(a, b, p, false); p = __builtin_amdgcn_cvt_pk_fp8_f32(c, d, p, true); return (unsigned)p; }
; DI void unpack8(const u32x4 w, float (&o)[8]) { o[0] = bf2f(w.x & 0xffffu); o[1] = bf2f(w.x >> 16); o[2] = bf2f(w.y & 0xffffu); o[3] = bf2f(w.y >> 16); o[4] = bf2f(w.z & 0xffffu); o[5] = bf2f(w.z >> 16); o[6] = bf2f(w.w & 0xffffu); o[7] = bf2f(w.w >> 16); }
; DI void phase_fin(const Frame& F, int j) {
;     ...
;             const int tt = t & (SEQ - 1); const bf16_t* pr = P + (size_t)t * AB_PROJ + 1024 + ch0; const float bs = BS[(size_t)t * 8 + (F.lane >> 3)];
;             float c[8], pv[8], nv[8]; unpack8(*(const u32x4*)pr, c); unpack8(*(const u32x4*)(pr - (tt > 0 ? AB_PROJ : 0)), pv); unpack8(*(const u32x4*)(pr + (tt < SEQ - 1 ? AB_PROJ : 0)), nv);
; #pragma unroll
;             for (int i = 0; i < 8; ++i) { const float p0 = tt > 0 ? pv[i] : 0.f, n0 = tt < SEQ - 1 ? nv[i] : 0.f; bo[i] = bs * (c[i] + mp[i] * (p0 - c[i]) + mn[i] * (n0 - c[i])); } }
;         float s = 0.f;
; #pragma unroll
;         for (int i = 0; i < 8; ++i) { yf[i] += yb[i]; s += yf[i]; }
;         const float mean = red8(s) * (1.f / 64.f); float q = 0.f;
; #pragma unroll
;         for (int i = 0; i < 8; ++i) { yf[i] -= mean; q += yf[i] * yf[i]; }
;         const float rstd = __builtin_amdgcn_rsqf(red8(q) * (1.f / 64.f) + eps64);
;         u32x2 w; float o[8];
; #pragma unroll
;         for (int i = 0; i < 8; ++i) o[i] = (yf[i] * rstd * lg[i] + lb[i] + bo[i]) * ga[i];
;         w.x = pk_fp8x4(o[0], o[1], o[2], o[3]); w.y = pk_fp8x4(o[4], o[5], o[6], o[7]);
;         *(u32x2*)(YAB + (size_t)t * D + ch0) = w;
	v_and_b32_e32 v73, 0xffff0000, v202
	v_lshlrev_b32_e32 v77, 16, v204
	v_and_b32_e32 v79, 0xffff0000, v204
	v_cndmask_b32_e64 v64, v73, 0, s[6:7]
	v_sub_f32_e32 v34, v64, v68
	v_lshlrev_b32_e32 v75, 16, v203
	v_mul_f32_e32 v89, v17, v34
	v_cndmask_b32_e64 v34, v36, 0, s[4:5]
	v_cndmask_b32_e64 v36, v75, 0, s[6:7]
	v_sub_f32_e32 v34, v34, v70
	v_mul_f32_e32 v64, v10, v34
	v_sub_f32_e32 v34, v36, v70
	v_and_b32_e32 v63, 0xffff0000, v203
	v_mul_f32_e32 v82, v18, v34
	v_cndmask_b32_e64 v34, v38, 0, s[4:5]
	v_cndmask_b32_e64 v36, v63, 0, s[6:7]
	v_sub_f32_e32 v34, v34, v72
	v_mul_f32_e32 v84, v11, v34
	v_sub_f32_e32 v34, v36, v72
	v_mul_f32_e32 v107, v19, v34
	v_cndmask_b32_e64 v34, v51, 0, s[4:5]
	v_cndmask_b32_e64 v36, v77, 0, s[6:7]
	v_sub_f32_e32 v34, v34, v74
	v_mul_f32_e32 v86, v12, v34
	v_sub_f32_e32 v34, v36, v74
	v_mul_f32_e32 v88, v20, v34
	v_cndmask_b32_e64 v34, v61, 0, s[4:5]
	v_cndmask_b32_e64 v36, v79, 0, s[6:7]
	v_sub_f32_e32 v34, v34, v76
	v_mul_f32_e32 v90, v13, v34
	v_sub_f32_e32 v34, v36, v76
	v_lshlrev_b32_e32 v81, 16, v205
	v_mul_f32_e32 v108, v21, v34
	v_cndmask_b32_e64 v34, v67, 0, s[4:5]
	v_cndmask_b32_e64 v36, v81, 0, s[6:7]
	v_sub_f32_e32 v34, v34, v78
	v_mul_f32_e32 v92, v14, v34
	v_sub_f32_e32 v34, v36, v78
	v_and_b32_e32 v65, 0xffff0000, v205
	v_mul_f32_e32 v94, v22, v34
	v_cndmask_b32_e64 v34, v69, 0, s[4:5]
	v_cndmask_b32_e64 v36, v65, 0, s[6:7]
	v_sub_f32_e32 v34, v34, v80
	v_mul_f32_e32 v96, v15, v34
	v_sub_f32_e32 v34, v36, v80
	v_mul_f32_e32 v109, v23, v34
	v_add_f32_e32 v34, 0, v99
	v_add_f32_e32 v34, v98, v34
	v_add_f32_e32 v34, v53, v34
	v_add_f32_e32 v34, v52, v34
	v_add_f32_e32 v34, v57, v34
	v_add_f32_e32 v34, v56, v34
	v_add_f32_e32 v34, v55, v34
	v_add_f32_e32 v34, v54, v34
	v_lshlrev_b32_e32 v71, 16, v202
	v_cndmask_b32_e64 v62, v71, 0, s[6:7]
	v_add_f32_dpp v34, v34, v34 quad_perm:[1,0,3,2] row_mask:0xf bank_mask:0xf bound_ctrl:1
	v_mov_b32_e32 v65, v53
	v_mov_b32_e32 v61, v99
	v_add_f32_dpp v34, v34, v34 quad_perm:[2,3,0,1] row_mask:0xf bank_mask:0xf bound_ctrl:1
	v_sub_f32_e32 v62, v62, v66
	v_add_f32_e32 v51, v84, v72
	v_add_f32_dpp v34, v34, v34 row_half_mirror row_mask:0xf bank_mask:0xf bound_ctrl:1
	v_mul_f32_e32 v79, 0x3c800000, v34
	v_mov_b32_e32 v81, v79
	v_mov_b32_e32 v75, v79
	v_mov_b32_e32 v71, v79
	v_mov_b32_e32 v73, v79
	v_mov_b32_e32 v67, v79
	v_pk_add_f32 v[58:59], v[92:93], v[78:79]
	v_pk_add_f32 v[92:93], v[92:93], v[78:79] neg_lo:[0,1] neg_hi:[0,1]
	v_add_f32_e32 v78, v96, v80
	v_pk_add_f32 v[54:55], v[96:97], v[80:81] neg_lo:[0,1] neg_hi:[0,1]
	v_pk_add_f32 v[96:97], v[86:87], v[74:75]
	v_pk_add_f32 v[74:75], v[86:87], v[74:75] neg_lo:[0,1] neg_hi:[0,1]
	v_pk_add_f32 v[86:87], v[64:65], v[70:71]
	v_pk_add_f32 v[64:65], v[64:65], v[70:71] neg_lo:[0,1] neg_hi:[0,1]
	v_pk_add_f32 v[52:53], v[84:85], v[72:73] neg_lo:[0,1] neg_hi:[0,1]
	v_pk_add_f32 v[60:61], v[60:61], v[66:67]
	v_pk_add_f32 v[66:67], v[98:99], v[66:67] neg_lo:[0,1] neg_hi:[0,1]
	v_mov_b32_e32 v69, v79
	v_mov_b32_e32 v77, v79
	v_mov_b32_e32 v70, v53
	v_mov_b32_e32 v71, v65
	v_add_f32_e32 v72, v83, v68
	v_pk_add_f32 v[68:69], v[98:99], v[68:69] op_sel_hi:[0,1] neg_lo:[0,1] neg_hi:[0,1]
	v_mul_f32_e32 v63, v67, v67
	v_pk_add_f32 v[56:57], v[90:91], v[76:77] neg_lo:[0,1] neg_hi:[0,1]
	v_pk_mul_f32 v[70:71], v[70:71], v[70:71]
	v_fmac_f32_e32 v63, v69, v69
	v_add_f32_e32 v100, v90, v76
	v_mov_b32_e32 v76, v57
	v_mov_b32_e32 v77, v75
	v_add_f32_e32 v63, v71, v63
	v_pk_mul_f32 v[76:77], v[76:77], v[76:77]
	v_add_f32_e32 v63, v70, v63
	v_mov_b32_e32 v80, v55
	v_mov_b32_e32 v81, v93
	v_add_f32_e32 v63, v77, v63
	v_pk_mul_f32 v[80:81], v[80:81], v[80:81]
	v_add_f32_e32 v63, v76, v63
	v_add_f32_e32 v63, v81, v63
	v_add_f32_e32 v63, v80, v63
	v_mul_f32_e32 v62, v16, v62
	v_mov_b32_e32 v38, v32
	v_add_f32_dpp v63, v63, v63 quad_perm:[1,0,3,2] row_mask:0xf bank_mask:0xf bound_ctrl:1
	v_mov_b32_e32 v36, v32
	v_mov_b32_e32 v34, v32
	v_add_f32_dpp v63, v63, v63 quad_perm:[2,3,0,1] row_mask:0xf bank_mask:0xf bound_ctrl:1
	s_nop 1
	v_add_f32_dpp v63, v63, v63 row_half_mirror row_mask:0xf bank_mask:0xf bound_ctrl:1
	v_fmamk_f32 v63, v63, 0x3c800000, v50
	v_rsq_f32_e32 v63, v63
	s_nop 0
	v_pk_add_f32 v[60:61], v[60:61], v[62:63]
	v_pk_mul_f32 v[66:67], v[66:67], v[62:63]
	v_mov_b32_e32 v83, v63
	v_mov_b32_e32 v61, v67
	v_pk_mul_f32 v[60:61], v[38:39], v[60:61]
	v_pk_mul_f32 v[66:67], v[68:69], v[62:63]
	v_add_f32_e32 v38, v0, v61
	v_add_f32_e32 v38, v60, v38
	v_mul_f32_e32 v38, v38, v24
	v_add_f32_e32 v60, v72, v89
	v_mov_b32_e32 v61, v67
	v_mov_b32_e32 v24, v32
	v_pk_mul_f32 v[60:61], v[24:25], v[60:61]
	v_pk_mul_f32 v[64:65], v[64:65], v[82:83]
	v_add_f32_e32 v24, v1, v61
	v_add_f32_e32 v24, v60, v24
	v_pk_add_f32 v[60:61], v[86:87], v[82:83]
	v_mul_f32_e32 v24, v24, v26
	v_mov_b32_e32 v61, v65
	v_pk_mul_f32 v[60:61], v[36:37], v[60:61]
	v_pk_mul_f32 v[52:53], v[52:53], v[62:63]
	v_add_f32_e32 v26, v2, v61
	v_add_f32_e32 v26, v60, v26
	v_mul_f32_e32 v36, v26, v28
	v_add_f32_e32 v60, v51, v107
	v_mov_b32_e32 v61, v53
	v_mov_b32_e32 v26, v32
	v_pk_mul_f32 v[52:53], v[26:27], v[60:61]
	v_mov_b32_e32 v89, v63
	v_add_f32_e32 v26, v3, v53
	v_add_f32_e32 v26, v52, v26
	v_pk_add_f32 v[52:53], v[96:97], v[88:89]
	v_pk_mul_f32 v[60:61], v[74:75], v[88:89]
	v_mul_f32_e32 v51, v26, v30
	v_mov_b32_e32 v53, v61
	v_pk_mul_f32 v[52:53], v[34:35], v[52:53]
	v_pk_mul_f32 v[56:57], v[56:57], v[62:63]
	v_add_f32_e32 v26, v4, v53
	v_add_f32_e32 v26, v52, v26
	v_add_f32_e32 v52, v100, v108
	v_mov_b32_e32 v53, v57
	v_mov_b32_e32 v28, v32
	v_pk_mul_f32 v[52:53], v[28:29], v[52:53]
	v_mul_f32_e32 v26, v26, v95
	v_add_f32_e32 v28, v5, v53
	v_mov_b32_e32 v95, v63
	v_add_f32_e32 v28, v52, v28
	v_pk_add_f32 v[52:53], v[58:59], v[94:95]
	v_pk_mul_f32 v[56:57], v[92:93], v[94:95]
	v_pk_mul_f32 v[54:55], v[54:55], v[62:63]
	v_mov_b32_e32 v53, v57
	v_pk_mul_f32 v[52:53], v[32:33], v[52:53]
	v_mul_f32_e32 v28, v28, v104
	v_add_f32_e32 v30, v6, v53
	v_add_f32_e32 v30, v52, v30
	v_mul_f32_e32 v34, v30, v105
	v_add_f32_e32 v52, v78, v109
	v_mov_b32_e32 v53, v55
	v_mov_b32_e32 v30, v32
	v_pk_mul_f32 v[52:53], v[30:31], v[52:53]
	v_lshl_add_u64 v[54:55], s[44:45], 0, v[48:49]
	v_add_f32_e32 v30, v7, v53
	v_add_f32_e32 v30, v52, v30
	v_mov_b32_e32 v52, v193
	v_mov_b32_e32 v53, v193
	v_cvt_pk_fp8_f32 v52, v38, v24
	v_cvt_pk_fp8_f32 v53, v26, v28
	v_mul_f32_e32 v30, v30, v106
	v_lshl_add_u64 v[48:49], v[48:49], 0, s[48:49]
	v_cvt_pk_fp8_f32 v52, v36, v51 op_sel:[0,0,1]
	v_cvt_pk_fp8_f32 v53, v34, v30 op_sel:[0,0,1]
	global_store_dwordx2 v[54:55], v[52:53], off
	s_cbranch_scc1 .LBB0_823
	v_readlane_b32 s50, v253, 50
	v_readlane_b32 s46, v253, 52
	v_readlane_b32 s51, v253, 51
	v_readlane_b32 s47, v253, 53
